# differential attention K tile: 4-bit XOR swizzle (conflict-free ds_read_b128 K fragments), own DMA offsets v247/v248; SB keeps 3-bit image
# speedup vs baseline: 1.0076x; 1.0076x over previous
; #define LAS __attribute__((address_space(3)))
; __device__ __forceinline__ int v_rd_base(int lane) { return ((lane & 3) << 3) | (((lane >> 2) & 3) << 6) | (((lane >> 4) & 1) << 5) | (((lane >> 5) & 1) << 8); }
; __device__ __forceinline__ AttDma att_dma_init(int wave, int lane) {
;     AttDma d;
; #pragma unroll
;     for (int i = 0; i < 2; ++i) { const int c = wave + 8 * i;
;         { const int row = 4 * c + (lane >> 4), ch = (lane & 15) ^ (row & 7); d.ko[i] = (unsigned)(row * HW + ch * 8) * 2u; }
;         { const int st = 2 * c + (lane >> 5), kk = (st >> 2) * 8 + ((lane & 31) >> 2), col = (st & 3) * 32 + 8 * (lane & 3);
;           const int k = (kk & ~0xC) | ((kk & 4) << 1) | ((kk & 8) >> 1); d.vo[i] = (unsigned)(k * HW + col) * 2u; } }
;     return d;
; __device__ __forceinline__ void da_unit(LAS unsigned char* lds, const bf16* __restrict__ Q, const bf16* __restrict__ Kp, const bf16* __restrict__ Vp, const float* __restrict__ gda, float lam, ...
;     constexpr float THR2 = 8.0f * 1.4426950408889634f;
;     const int r32 = lane & 31, hi = lane >> 5, rg = wave & 3, comp = wave >> 2;
;     LAS unsigned char* V_lds = lds; LAS unsigned char* K_lds = lds + 4 * SHM_T; LAS float* X = (LAS float*)lds;
;     LAS float* wsf = (LAS float*)(lds + MISC_OFF + 2048) + wave * 64; LAS float* li_l = wsf; LAS float* al_l = wsf + 32;
;     const int m0 = b * SEQ + 128 * qt;
;     bf16x8 qr[4];
;     { const bf16* Qw = Q + (size_t)(m0 + 32 * rg + r32) * HW + h * 128 + comp * 64 + hi * 8;
; #pragma unroll
;       for (int d0 = 0; d0 < 4; ++d0) qr[d0] = *(const bf16x8*)(Qw + d0 * 16); }
;     const bf16* Kh = Kp + (size_t)(b * LPB) * HW + h * 128; const bf16* Vh = Vp + (size_t)(b * LPB) * HW + h * 128;
;     const int vb0 = (int)(unsigned)(uintptr_t)V_lds + v_rd_base(lane);
;     const int NT = 2 * qt + 3, NTw = 2 * qt + 2 + (rg >> 1);
;     const AttDma dm = att_dma_init(wave, lane);
.LBB0_564:
	s_cmpk_gt_i32 s0, 0xff
	v_lshlrev_b32_e32 v1, 3, v0
	s_waitcnt lgkmcnt(0)
	v_lshrrev_b32_e32 v133, 4, v194
	s_cbranch_scc1 .LBB0_627
	v_mov_b32_e32 v147, 0
	global_load_dword v168, v147, s[92:93] offset:64
	s_add_u32 s2, s92, 0x8200000
	s_addc_u32 s3, s93, 0
	s_add_u32 s61, s92, 0xe400000
	s_addc_u32 s62, s93, 0
	s_add_u32 s63, s92, 0x10500000
	v_readlane_b32 s9, v246, 33
	s_addc_u32 s71, s93, 0
	s_waitcnt vmcnt(23)
	v_bfe_u32 v6, v194, 2, 2
	v_lshrrev_b32_e32 v8, 1, v194
	s_lshl_b32 s53, s9, 2
	v_and_b32_e32 v5, 15, v0
	v_and_or_b32 v6, v8, 8, v6
	v_or_b32_e32 v8, s53, v133
	s_lshl_b32 s54, s9, 1
	v_lshrrev_b32_e32 v164, 5, v194
	v_bitop3_b32 v9, v8, v5, 7 bitop3:0x6c
	v_bitop3_b32 v249, v8, v5, 15 bitop3:0x6c
	v_lshlrev_b32_e32 v8, 11, v8
	s_and_b32 s6, s53, 0x1ffff0
	s_and_b32 s7, s54, 4
	v_lshl_or_b32 v135, v9, 4, v8
	v_lshl_or_b32 v247, v249, 4, v8
	v_or_b32_e32 v8, s54, v164
	s_or_b32 s6, s7, s6
	v_lshlrev_b32_e32 v3, 4, v194
	v_lshlrev_b32_e32 v8, 6, v8
	v_or_b32_e32 v9, s6, v6
	s_add_i32 s6, s9, 8
	v_and_b32_e32 v7, 48, v3
	v_and_b32_e32 v8, 0xc0, v8
	v_lshlrev_b32_e32 v9, 11, v9
	s_lshl_b32 s55, s6, 2
	s_lshl_b32 s56, s6, 1
	v_or3_b32 v137, v9, v8, v7
	v_or_b32_e32 v8, s55, v133
	s_and_b32 s6, s55, 0x1ffff0
	s_and_b32 s7, s56, 4
	v_readlane_b32 s14, v246, 8
	v_lshlrev_b32_e32 v4, 1, v0
	v_bitop3_b32 v9, v8, v5, 7 bitop3:0x6c
	v_bitop3_b32 v249, v8, v5, 15 bitop3:0x6c
	v_lshlrev_b32_e32 v8, 11, v8
	s_or_b32 s6, s7, s6
	s_lshr_b32 s0, s14, 8
	s_lshl_b32 s1, s9, 8
	v_and_b32_e32 v161, 0xc0, v3
	v_and_b32_e32 v162, 32, v4
	v_and_b32_e32 v163, 0x118, v1
	v_lshl_or_b32 v139, v9, 4, v8
	v_lshl_or_b32 v248, v249, 4, v8
	v_or_b32_e32 v8, s56, v164
	v_or_b32_e32 v6, s6, v6
	s_lshl_b32 s6, s9, 10
	s_bfe_u32 s5, s14, 0x20006
	s_add_i32 s74, s1, 0
	s_lshl_b32 s4, s0, 6
	v_lshlrev_b32_e32 v2, 3, v164
	v_or3_b32 v4, v162, v163, v161
	s_bfe_u32 s1, s9, 0x10001
	v_lshlrev_b32_e32 v8, 6, v8
	s_add_i32 s60, 0, 0x10000
	s_add_i32 s57, s6, 0
	s_add_i32 s7, s6, 0x2000
	s_add_i32 s80, 0, 0x14000
	s_add_i32 s74, s74, 0x20800
	s_lshl_b32 s75, s5, 5
	v_and_b32_e32 v8, 0xc0, v8
	v_lshlrev_b32_e32 v6, 11, v6
	s_add_i32 s76, s60, s6
	s_add_i32 s77, s60, s7
	s_add_i32 s58, s57, 0x2000
	s_add_i32 s78, s80, s6
	s_add_i32 s79, s57, 0x4000
	s_add_i32 s80, s80, s7
	s_add_i32 s81, s57, 0x6000
	v_add_u32_e32 v169, 0, v4
	s_or_b32 s82, s1, 2
	v_or_b32_e32 v4, s4, v2
	v_and_b32_e32 v131, 31, v0
	v_or3_b32 v141, v6, v8, v7
	s_cmp_eq_u32 s0, 1
	s_movk_i32 s8, 0xf0
	v_mov_b32_e32 v6, 0x2000
	v_lshlrev_b32_e32 v4, 1, v4
	s_cselect_b64 s[12:13], -1, 0
	v_and_b32_e32 v166, 0x70, v3
	v_and_b32_e32 v249, 0xf0, v3
	v_lshl_or_b32 v170, v194, 8, v6
	v_lshlrev_b32_e32 v6, 2, v131
	s_cmpk_gt_u32 s14, 0xff
	v_bitop3_b32 v173, v4, v3, s8 bitop3:0x78
	v_lshlrev_b32_e32 v3, 11, v164
	s_cselect_b64 s[34:35], -1, 0
	s_cmpk_lt_u32 s14, 0x100
	v_add3_u32 v3, 0, v6, v3
	s_cselect_b64 s[44:45], -1, 0
	v_lshl_add_u32 v177, s5, 14, v3
	s_lshl_b32 s5, s9, 13
	v_add_u32_e32 v172, s60, v170
	s_add_i32 s60, s60, s5
	v_add_u32_e32 v180, s52, v3
	v_or_b32_e32 v3, 4, v133
	v_lshl_add_u32 v149, v3, 8, s60
	v_lshlrev_b32_e32 v132, 11, v3
	v_or_b32_e32 v3, 8, v133
	v_lshl_add_u32 v153, v3, 8, s60
	v_lshlrev_b32_e32 v134, 11, v3
	v_or_b32_e32 v3, 12, v133
	s_add_i32 s84, 0, 0x18000
	v_lshl_add_u32 v154, v3, 8, s60
	v_lshlrev_b32_e32 v136, 11, v3
	v_or_b32_e32 v3, 16, v133
	s_add_i32 s83, s84, s6
	s_movk_i32 s6, 0x60
	v_lshl_add_u32 v155, v3, 8, s60
	v_lshlrev_b32_e32 v138, 11, v3
	v_or_b32_e32 v3, 20, v133
	v_add_u32_e32 v171, s74, v6
	v_bitop3_b32 v174, v4, v249, 32 bitop3:0x36
	v_bitop3_b32 v175, v4, v249, 64 bitop3:0x36
	v_bitop3_b32 v176, v4, v249, s6 bitop3:0x36
	v_lshlrev_b32_e32 v4, 10, v164
	v_lshlrev_b32_e32 v6, 1, v131
	v_lshlrev_b32_e32 v179, 6, v164
	v_lshl_add_u32 v156, v3, 8, s60
	v_lshlrev_b32_e32 v140, 11, v3
	v_or_b32_e32 v3, 24, v133
	v_add3_u32 v178, s60, v4, v6
	v_xor_b32_e32 v4, 64, v179
	v_lshlrev_b32_e32 v143, 4, v5
	v_lshl_add_u32 v157, v3, 8, s60
	v_lshlrev_b32_e32 v142, 11, v3
	v_or_b32_e32 v3, 28, v133
	v_lshlrev_b32_e32 v146, 1, v2
	v_mbcnt_lo_u32_b32 v2, -1, 0
	s_mov_b32 s17, 0
	v_lshlrev_b32_e32 v165, 8, v131
	v_cmp_gt_u32_e64 s[0:1], 32, v194
	v_lshlrev_b32_e32 v167, 4, v164
	s_add_i32 s33, s57, 0x8000
	s_add_i32 s84, s84, s7
	s_add_i32 s59, s57, 0xa000
	v_lshlrev_b32_e32 v148, 3, v5
	v_lshl_add_u32 v145, v133, 8, s60
	v_lshlrev_b32_e32 v130, 11, v133
	v_xor_b32_e32 v152, 64, v143
	v_lshl_add_u32 v158, v3, 8, s60
	v_lshlrev_b32_e32 v144, 11, v3
	s_lshl_b32 s68, s4, 1
	s_mov_b32 s7, 0x20000
	s_brev_b32 s6, -2
	s_mov_b32 s85, 0x40000
	s_mov_b32 s70, 0x3f4ccccd
	v_mov_b32_e32 v181, 0x3727c5ac
	v_add_u32_e32 v159, v178, v4
	v_mbcnt_hi_u32_b32 v160, -1, v2
	v_readlane_b32 s86, v246, 13
	s_branch .LBB0_567

; #define LAS __attribute__((address_space(3)))
; __device__ __forceinline__ void da_unit(LAS unsigned char* lds, const bf16* __restrict__ Q, const bf16* __restrict__ Kp, const bf16* __restrict__ Vp, const float* __restrict__ gda, float lam, ...
;     ...
;     bf16x8 qr[4];
;     { const bf16* Qw = Q + (size_t)(m0 + 32 * rg + r32) * HW + h * 128 + comp * 64 + hi * 8;
; #pragma unroll
;       for (int d0 = 0; d0 < 4; ++d0) qr[d0] = *(const bf16x8*)(Qw + d0 * 16); }
;     const bf16* Kh = Kp + (size_t)(b * LPB) * HW + h * 128; const bf16* Vh = Vp + (size_t)(b * LPB) * HW + h * 128;
;     const int vb0 = (int)(unsigned)(uintptr_t)V_lds + v_rd_base(lane);
;     const int NT = 2 * qt + 3, NTw = 2 * qt + 2 + (rg >> 1);
;     const AttDma dm = att_dma_init(wave, lane);
;     att_dma(dm, Kh, Vh, 0, K_lds, V_lds, wave);
;     att_dma(dm, Kh, Vh, 64, K_lds + SHM_T, V_lds + SHM_T, wave);
;     ...
;         if (j + 1 < NT) asm volatile("s_waitcnt vmcnt(4)" ::: "memory"); else asm volatile("s_waitcnt vmcnt(0)" ::: "memory");
;         __syncthreads();
;         if (j + 2 < NT) att_dma(dm, Kh, Vh, (j + 2) * 64, K_lds + (kbuf == 0 ? 2 : kbuf - 1) * SHM_T, V_lds + ((vbuf + 2) & 3) * SHM_T, wave);
;         if (comp == 1 && pend) { pv_pipe(o, vb0 + pbuf * SHM_T, pa0, pa1, pa2, pa3); pend = false; }
;         if (j < NTw) {
;             f32x16 p0 = mneg, p1 = mneg;
;             { const LAS unsigned char* Ks = K_lds + buf * SHM_T; bf16x8 kb0[4], kb1[4];
; #pragma unroll
;               for (int d0 = 0; d0 < 4; ++d0) { const int cb = (comp * 64 + d0 * 16 + hi * 8) * 2;
;                   kb0[d0] = *(const LAS bf16x8*)(Ks + KSWZ(r32, cb)); kb1[d0] = *(const LAS bf16x8*)(Ks + KSWZ(32 + r32, cb)); }
;               SBAR();
; #pragma unroll
;               for (int d0 = 0; d0 < 4; ++d0) { p0 = __builtin_amdgcn_mfma_f32_32x32x16_bf16(kb0[d0], qr[d0], p0, 0, 0, 0); p1 = __builtin_amdgcn_mfma_f32_32x32x16_bf16(kb1[d0], qr[d0], p1, 0, 0, 0); } }
;             if (j == 0) {
; #pragma unroll
;                 for (int r = 0; r < 16; ++r) p0[r] = -INFINITY;
; #pragma unroll
;                 for (int r = 0; r < 8; ++r) p1[r] = -INFINITY;
;             }
;             float pmax = p0[0];
; #pragma unroll
;             for (int r = 1; r < 16; ++r) pmax = fmaxf(pmax, p0[r]);
; #pragma unroll
;             for (int r = 0; r < 16; ++r) pmax = fmaxf(pmax, p1[r]);
.LBB0_569:
	s_and_b32 s4, s95, 2
	s_or_b32 s96, s88, s4
	s_bitcmp0_b32 s95, 0
	s_cselect_b32 s73, s87, s89
	s_lshl_b32 s4, s73, 7
	s_or_b32 s72, s4, s90
	v_or_b32_e32 v2, s72, v131
	v_ashrrev_i32_e32 v3, 31, v2
	v_lshlrev_b64 v[2:3], 11, v[2:3]
	s_lshl_b32 s16, s96, 8
	v_lshl_add_u64 v[2:3], s[2:3], 0, v[2:3]
	s_add_u32 s4, s91, s16
	v_lshl_add_u64 v[2:3], v[2:3], 0, s[16:17]
	s_mov_b32 s69, s17
	s_addc_u32 s5, s92, 0
	v_lshl_add_u64 v[2:3], v[2:3], 0, s[68:69]
	s_add_u32 s64, s93, s16
	s_mov_b32 m0, s76
	v_lshl_add_u64 v[2:3], v[2:3], 0, v[146:147]
	s_addc_u32 s8, s94, 0
	s_and_b32 s5, s5, 0xffff
	global_load_dwordx4 v[114:117], v[2:3], off
	global_load_dwordx4 v[118:121], v[2:3], off offset:32
	global_load_dwordx4 v[122:125], v[2:3], off offset:64
	global_load_dwordx4 v[126:129], v[2:3], off offset:96
	s_and_b32 s65, s8, 0xffff
	s_mov_b32 s66, s6
	s_mov_b32 s67, s7
	buffer_load_dwordx4 v247, s[4:7], 0 offen lds
	s_mov_b32 m0, s57
	v_add_u32_e32 v2, v172, v173
	buffer_load_dwordx4 v137, s[64:67], 0 offen lds
	s_mov_b32 m0, s77
	v_add_u32_e32 v6, v172, v174
	buffer_load_dwordx4 v248, s[4:7], 0 offen lds
	s_mov_b32 m0, s58
	s_waitcnt vmcnt(29)
	v_add_u32_e32 v10, v172, v175
	buffer_load_dwordx4 v141, s[64:67], 0 offen lds
	s_mov_b32 m0, s78
	s_waitcnt vmcnt(29)
	v_add_u32_e32 v14, v172, v176
	buffer_load_dwordx4 v247, s[4:7], s7 offen lds
	s_mov_b32 m0, s79
	s_nop 0
	buffer_load_dwordx4 v137, s[64:67], s7 offen lds
	s_mov_b32 m0, s80
	s_nop 0
	buffer_load_dwordx4 v248, s[4:7], s7 offen lds
	s_mov_b32 m0, s81
	s_nop 0
	buffer_load_dwordx4 v141, s[64:67], s7 offen lds
	s_mov_b32 m0, s83
	s_waitcnt vmcnt(4)
	s_barrier
	buffer_load_dwordx4 v247, s[4:7], s85 offen lds
	s_mov_b32 m0, s33
	s_nop 0
	buffer_load_dwordx4 v137, s[64:67], s85 offen lds
	s_mov_b32 m0, s84
	s_nop 0
	buffer_load_dwordx4 v248, s[4:7], s85 offen lds
	s_mov_b32 m0, s59
	s_nop 0
	buffer_load_dwordx4 v141, s[64:67], s85 offen lds
	ds_read_b128 v[2:5], v2
	ds_read_b128 v[6:9], v6
	ds_read_b128 v[10:13], v10
	ds_read_b128 v[34:37], v14
	s_waitcnt lgkmcnt(3)
	v_mfma_f32_32x32x16_bf16 v[18:33], v[2:5], v[114:117], 0
	s_mov_b32 s8, 0xff800000
	s_mov_b32 s16, s17
	s_mov_b32 s18, s17
	s_mov_b32 s19, s17
	s_mov_b32 s20, s17
	s_mov_b32 s21, s17
	s_mov_b32 s22, s17
	s_waitcnt lgkmcnt(2)
	v_mfma_f32_32x32x16_bf16 v[18:33], v[6:9], v[118:121], v[18:33]
	s_mov_b32 s23, s17
	s_mov_b32 s24, s17
	s_mov_b32 s25, s17
	s_mov_b32 s26, s17
	s_mov_b32 s27, s17
	s_mov_b32 s28, s17
	s_mov_b32 s29, s17
	s_waitcnt lgkmcnt(1)
	v_mfma_f32_32x32x16_bf16 v[18:33], v[10:13], v[122:125], v[18:33]
	s_mov_b32 s30, s17
	s_mov_b32 s31, s17
	v_mov_b64_e32 v[2:3], s[16:17]
	v_mov_b64_e32 v[16:17], s[30:31]
	v_mov_b64_e32 v[4:5], s[18:19]
	v_mov_b64_e32 v[6:7], s[20:21]
	v_mov_b64_e32 v[8:9], s[22:23]
	s_waitcnt lgkmcnt(0)
	v_mfma_f32_32x32x16_bf16 v[18:33], v[34:37], v[126:129], v[18:33]
	v_mov_b64_e32 v[10:11], s[24:25]
	v_mov_b64_e32 v[12:13], s[26:27]
	v_mov_b64_e32 v[14:15], s[28:29]
	v_mov_b64_e32 v[48:49], v[16:17]
	v_mov_b64_e32 v[64:65], v[16:17]
	s_and_b64 vcc, exec, s[44:45]
	v_mov_b64_e32 v[46:47], v[14:15]
	s_nop 4
	v_max3_f32 v18, v26, s8, v27
	v_max3_f32 v18, v18, v28, v29
	v_max3_f32 v18, v18, v30, v31
	v_max3_f32 v67, v18, v32, v33
	v_mov_b32_e32 v18, v67
	s_nop 1
	v_permlane32_swap_b32_e32 v67, v18
	v_sub_f32_e32 v18, 0xff800000, v67
	v_exp_f32_e32 v18, v18
	v_sub_f32_e32 v20, v27, v67
	v_sub_f32_e32 v19, v26, v67
	v_exp_f32_e32 v19, v19
	v_add_f32_e32 v27, 0, v18
	v_add_f32_e32 v27, v18, v27
	v_add_f32_e32 v27, v18, v27
	v_add_f32_e32 v27, v18, v27
	v_add_f32_e32 v27, v18, v27
	v_add_f32_e32 v27, v18, v27
	v_add_f32_e32 v27, v18, v27
	v_add_f32_e32 v27, v18, v27
	v_add_f32_e32 v27, v18, v27
	v_add_f32_e32 v27, v18, v27
	v_add_f32_e32 v27, v18, v27
	v_add_f32_e32 v27, v18, v27
	v_add_f32_e32 v27, v18, v27
	v_add_f32_e32 v27, v18, v27
	v_add_f32_e32 v27, v18, v27
	v_add_f32_e32 v27, v18, v27
	v_add_f32_e32 v27, v18, v27
	v_add_f32_e32 v27, v18, v27
	v_add_f32_e32 v27, v18, v27
	v_add_f32_e32 v27, v18, v27
	v_add_f32_e32 v27, v18, v27
	v_sub_f32_e32 v21, v28, v67
	v_exp_f32_e32 v20, v20
	v_add_f32_e32 v27, v18, v27
	v_sub_f32_e32 v22, v29, v67
	v_exp_f32_e32 v21, v21
	v_add_f32_e32 v27, v18, v27
	v_sub_f32_e32 v23, v30, v67
	v_exp_f32_e32 v22, v22
	v_add_f32_e32 v27, v18, v27
	v_sub_f32_e32 v24, v31, v67
	v_exp_f32_e32 v23, v23
	v_add_f32_e32 v27, v19, v27
	v_sub_f32_e32 v25, v32, v67
	v_exp_f32_e32 v24, v24
	v_add_f32_e32 v27, v20, v27
	v_sub_f32_e32 v26, v33, v67
	v_exp_f32_e32 v25, v25
	v_add_f32_e32 v27, v21, v27
	v_exp_f32_e32 v26, v26
	v_add_f32_e32 v27, v22, v27
	v_add_f32_e32 v27, v23, v27
	v_add_f32_e32 v27, v24, v27
	v_add_f32_e32 v27, v25, v27
	v_add_f32_e32 v66, v26, v27
	v_mov_b32_e32 v27, v66
	v_cvt_pk_bf16_f32 v86, v18, v18
	s_nop 0
	v_permlane32_swap_b32_e32 v66, v27
	v_mov_b32_e32 v88, v86
	s_nop 1
	v_permlane32_swap_b32_e32 v86, v88
	v_cvt_pk_bf16_f32 v82, v19, v20
	v_cvt_pk_bf16_f32 v83, v21, v22
	v_cvt_pk_bf16_f32 v84, v23, v24
	v_cvt_pk_bf16_f32 v85, v25, v26
	v_mov_b64_e32 v[32:33], v[16:17]
	v_mov_b32_e32 v87, v86
	v_mov_b32_e32 v89, v88
	v_permlane32_swap_b32_e32 v82, v84
	v_permlane32_swap_b32_e32 v83, v85
	v_mov_b64_e32 v[30:31], v[14:15]
	v_mov_b64_e32 v[28:29], v[12:13]
	v_mov_b64_e32 v[26:27], v[10:11]
	v_mov_b64_e32 v[24:25], v[8:9]
	v_mov_b64_e32 v[22:23], v[6:7]
	v_mov_b64_e32 v[20:21], v[4:5]
	v_mov_b64_e32 v[18:19], v[2:3]
	v_mov_b64_e32 v[44:45], v[12:13]
	v_mov_b64_e32 v[42:43], v[10:11]
	v_mov_b64_e32 v[40:41], v[8:9]
	v_mov_b64_e32 v[38:39], v[6:7]
	v_mov_b64_e32 v[36:37], v[4:5]
	v_mov_b64_e32 v[34:35], v[2:3]
	v_mov_b64_e32 v[62:63], v[14:15]
	v_mov_b64_e32 v[60:61], v[12:13]
	v_mov_b64_e32 v[58:59], v[10:11]
	v_mov_b64_e32 v[56:57], v[8:9]
	v_mov_b64_e32 v[54:55], v[6:7]
	v_mov_b64_e32 v[52:53], v[4:5]
	v_mov_b64_e32 v[50:51], v[2:3]
	s_cbranch_vccz .LBB0_571
; #define SBAR() __builtin_amdgcn_sched_barrier(0)
; #define ATT_RDK(X, KS) do { X##0 = tr_read<v_rd_off(0, KS, 0)>(vb); X##1 = tr_read<v_rd_off(0, KS, 1)>(vb); X##2 = tr_read<v_rd_off(1, KS, 0)>(vb); X##3 = tr_read<v_rd_off(1, KS, 1)>(vb); \
;     X##4 = tr_read<v_rd_off(2, KS, 0)>(vb); X##5 = tr_read<v_rd_off(2, KS, 1)>(vb); X##6 = tr_read<v_rd_off(3, KS, 0)>(vb); X##7 = tr_read<v_rd_off(3, KS, 1)>(vb); } while (0)
; #define ATT_MMAK(PA, X) do { o[0] = __builtin_amdgcn_mfma_f32_32x32x16_bf16(PA, ATT_PKV(X##0, X##1), o[0], 0, 0, 0); o[1] = __builtin_amdgcn_mfma_f32_32x32x16_bf16(PA, ATT_PKV(X##2, X##3), o[1], 0, 0, 0); \
;     o[2] = __builtin_amdgcn_mfma_f32_32x32x16_bf16(PA, ATT_PKV(X##4, X##5), o[2], 0, 0, 0); o[3] = __builtin_amdgcn_mfma_f32_32x32x16_bf16(PA, ATT_PKV(X##6, X##7), o[3], 0, 0, 0); } while (0)
; __device__ __forceinline__ void pv_pipe(f32x16* o, int vb, bf16x8 pa0, bf16x8 pa1, bf16x8 pa2, bf16x8 pa3) {
;     s16x4 a0, a1, a2, a3, a4, a5, a6, a7, b0, b1, b2, b3, b4, b5, b6, b7;
;     SBAR(); ATT_RDK(a, 0); ATT_RDK(b, 1);
;     asm volatile("s_waitcnt lgkmcnt(8)" ::: "memory"); SBAR(); ATT_MMAK(pa0, a);
;     SBAR(); ATT_RDK(a, 2);
;     asm volatile("s_waitcnt lgkmcnt(8)" ::: "memory"); SBAR(); ATT_MMAK(pa1, b);
;     SBAR(); ATT_RDK(b, 3);
;     asm volatile("s_waitcnt lgkmcnt(8)" ::: "memory"); SBAR(); ATT_MMAK(pa2, a);
;     asm volatile("s_waitcnt lgkmcnt(0)" ::: "memory"); SBAR(); ATT_MMAK(pa3, b);
; }
	ds_read_b64_tr_b16 v[2:3], v169 offset:0
	ds_read_b64_tr_b16 v[4:5], v169 offset:0x800
	ds_read_b64_tr_b16 v[18:19], v169 offset:0x200
	ds_read_b64_tr_b16 v[20:21], v169 offset:0xa00
	ds_read_b64_tr_b16 v[34:35], v169 offset:0x400
	ds_read_b64_tr_b16 v[36:37], v169 offset:0xc00
	ds_read_b64_tr_b16 v[50:51], v169 offset:0x600
	ds_read_b64_tr_b16 v[52:53], v169 offset:0xe00
	ds_read_b64_tr_b16 v[68:69], v169 offset:0x1000
	ds_read_b64_tr_b16 v[70:71], v169 offset:0x1800
	ds_read_b64_tr_b16 v[72:73], v169 offset:0x1200
	ds_read_b64_tr_b16 v[74:75], v169 offset:0x1a00
	ds_read_b64_tr_b16 v[76:77], v169 offset:0x1400
	ds_read_b64_tr_b16 v[78:79], v169 offset:0x1c00
	ds_read_b64_tr_b16 v[90:91], v169 offset:0x1600
	ds_read_b64_tr_b16 v[92:93], v169 offset:0x1e00
	s_waitcnt lgkmcnt(8)
	s_nop 0
	v_mfma_f32_32x32x16_bf16 v[2:17], v[86:89], v[2:5], 0
	v_mfma_f32_32x32x16_bf16 v[18:33], v[86:89], v[18:21], 0
	v_mfma_f32_32x32x16_bf16 v[34:49], v[86:89], v[34:37], 0
	v_mfma_f32_32x32x16_bf16 v[50:65], v[86:89], v[50:53], 0
	ds_read_b64_tr_b16 v[94:95], v169 offset:0x2000
	ds_read_b64_tr_b16 v[96:97], v169 offset:0x2800
	ds_read_b64_tr_b16 v[98:99], v169 offset:0x2200
	ds_read_b64_tr_b16 v[100:101], v169 offset:0x2a00
	ds_read_b64_tr_b16 v[102:103], v169 offset:0x2400
	ds_read_b64_tr_b16 v[104:105], v169 offset:0x2c00
	ds_read_b64_tr_b16 v[106:107], v169 offset:0x2600
	ds_read_b64_tr_b16 v[108:109], v169 offset:0x2e00
	s_waitcnt lgkmcnt(8)
	v_mfma_f32_32x32x16_bf16 v[2:17], v[86:89], v[68:71], v[2:17]
	v_mfma_f32_32x32x16_bf16 v[18:33], v[86:89], v[72:75], v[18:33]
	v_mfma_f32_32x32x16_bf16 v[34:49], v[86:89], v[76:79], v[34:49]
	v_mfma_f32_32x32x16_bf16 v[50:65], v[86:89], v[90:93], v[50:65]
	ds_read_b64_tr_b16 v[68:69], v169 offset:0x3000
	ds_read_b64_tr_b16 v[70:71], v169 offset:0x3800
	ds_read_b64_tr_b16 v[72:73], v169 offset:0x3200
	ds_read_b64_tr_b16 v[74:75], v169 offset:0x3a00
	ds_read_b64_tr_b16 v[76:77], v169 offset:0x3400
	ds_read_b64_tr_b16 v[78:79], v169 offset:0x3c00
	ds_read_b64_tr_b16 v[90:91], v169 offset:0x3600
	ds_read_b64_tr_b16 v[92:93], v169 offset:0x3e00
	s_waitcnt lgkmcnt(8)
	v_mfma_f32_32x32x16_bf16 v[2:17], v[86:89], v[94:97], v[2:17]
	s_waitcnt lgkmcnt(0)
	v_mfma_f32_32x32x16_bf16 v[18:33], v[86:89], v[98:101], v[18:33]
	v_mfma_f32_32x32x16_bf16 v[34:49], v[86:89], v[102:105], v[34:49]
	v_mfma_f32_32x32x16_bf16 v[50:65], v[86:89], v[106:109], v[50:65]
	v_mfma_f32_32x32x16_bf16 v[2:17], v[82:85], v[68:71], v[2:17]
	v_mfma_f32_32x32x16_bf16 v[18:33], v[82:85], v[72:75], v[18:33]
	v_mfma_f32_32x32x16_bf16 v[34:49], v[82:85], v[76:79], v[34:49]
	v_mfma_f32_32x32x16_bf16 v[50:65], v[82:85], v[90:93], v[50:65]

; #define LAS __attribute__((address_space(3)))
; __device__ __forceinline__ void att_dma(const AttDma& d, const bf16* __restrict__ Kh, const bf16* __restrict__ Vh, int key0, LAS unsigned char* Kdst, LAS unsigned char* Vdst, int wave) {
;     const __amdgpu_buffer_rsrc_t rk = __builtin_amdgcn_make_buffer_rsrc((void*)Kh, 0, 0x7fffffff, 0x00020000), rv = __builtin_amdgcn_make_buffer_rsrc((void*)Vh, 0, 0x7fffffff, 0x00020000);
;     const int so = key0 * HW * 2;
; #pragma unroll
;     for (int i = 0; i < 2; ++i) { const int c = wave + 8 * i;
;         __builtin_amdgcn_raw_ptr_buffer_load_lds(rk, (LAS void*)(Kdst + c * 1024), 16, (int)d.ko[i], so, 0, 0);
;         __builtin_amdgcn_raw_ptr_buffer_load_lds(rv, (LAS void*)(Vdst + c * 1024), 16, (int)d.vo[i], so, 0, 0); }
; }
; __device__ __forceinline__ void da_unit(LAS unsigned char* lds, const bf16* __restrict__ Q, const bf16* __restrict__ Kp, const bf16* __restrict__ Vp, const float* __restrict__ gda, float lam, ...
;     ...
;         if (j + 1 < NT) asm volatile("s_waitcnt vmcnt(4)" ::: "memory"); else asm volatile("s_waitcnt vmcnt(0)" ::: "memory");
;         __syncthreads();
;         if (j + 2 < NT) att_dma(dm, Kh, Vh, (j + 2) * 64, K_lds + (kbuf == 0 ? 2 : kbuf - 1) * SHM_T, V_lds + ((vbuf + 2) & 3) * SHM_T, wave);
.LBB0_579:
	s_add_i32 s8, s27, 5
	s_cmp_ge_u32 s8, s24
	s_barrier
	s_cbranch_scc1 .LBB0_582
	s_lshl_b32 s8, s23, 14
	s_addk_i32 s8, 0xc000
	s_cmp_lg_u32 s23, 0
	s_cselect_b32 s8, s8, 0x8000
	s_lshl_b32 s9, s29, 14
	s_xor_b32 s9, s9, 0x8000
	s_add_i32 s8, s76, s8
	s_mov_b32 m0, s8
	s_add_i32 s9, s57, s9
	buffer_load_dwordx4 v247, s[4:7], s28 offen lds
	s_mov_b32 s66, s6
	s_mov_b32 s67, s7
	s_mov_b32 m0, s9
	s_nop 0
	buffer_load_dwordx4 v137, s[64:67], s28 offen lds
	s_add_i32 m0, s8, 0x2000
	s_nop 0
	buffer_load_dwordx4 v248, s[4:7], s28 offen lds
	s_add_i32 m0, s9, 0x2000
	s_nop 0
	buffer_load_dwordx4 v141, s[64:67], s28 offen lds
	s_and_b64 s[8:9], s[12:13], s[18:19]
	s_andn2_b64 vcc, exec, s[8:9]
	s_cbranch_vccz .LBB0_583

; __global__ void __launch_bounds__(NWAVES * 64, 2) fwd(Args args) {
	.amdhsa_kernel _Z3fwd4Args
		.amdhsa_group_segment_fixed_size 0
		.amdhsa_private_segment_fixed_size 0
		.amdhsa_kernarg_size 432
		.amdhsa_user_sgpr_count 2
		.amdhsa_user_sgpr_dispatch_ptr 0
		.amdhsa_user_sgpr_queue_ptr 0
		.amdhsa_user_sgpr_kernarg_segment_ptr 1
		.amdhsa_user_sgpr_dispatch_id 0
		.amdhsa_user_sgpr_kernarg_preload_length 0
		.amdhsa_user_sgpr_kernarg_preload_offset 0
		.amdhsa_user_sgpr_private_segment_size 0
		.amdhsa_uses_dynamic_stack 0
		.amdhsa_enable_private_segment 0
		.amdhsa_system_sgpr_workgroup_id_x 1
		.amdhsa_system_sgpr_workgroup_id_y 0
		.amdhsa_system_sgpr_workgroup_id_z 0
		.amdhsa_system_sgpr_workgroup_info 0
		.amdhsa_system_vgpr_workitem_id 0
		.amdhsa_next_free_vgpr 250
		.amdhsa_next_free_sgpr 98
		.amdhsa_accum_offset 252
		.amdhsa_reserve_vcc 1
		.amdhsa_float_round_mode_32 0
		.amdhsa_float_round_mode_16_64 0
		.amdhsa_float_denorm_mode_32 3
		.amdhsa_float_denorm_mode_16_64 3
		.amdhsa_dx10_clamp 1
		.amdhsa_ieee_mode 1
		.amdhsa_fp16_overflow 0
		.amdhsa_tg_split 0
		.amdhsa_exception_fp_ieee_invalid_op 0
		.amdhsa_exception_fp_denorm_src 0
		.amdhsa_exception_fp_ieee_div_zero 0
		.amdhsa_exception_fp_ieee_overflow 0
		.amdhsa_exception_fp_ieee_underflow 0
		.amdhsa_exception_fp_ieee_inexact 0
		.amdhsa_exception_int_div_zero 0
	.end_amdhsa_kernel

; __global__ void __launch_bounds__(NWAVES * 64, 2) fwd(Args args) {
amdhsa.kernels:
  - .agpr_count:     0
    .args:
      - .offset:         0
        .size:           176
        .value_kind:     by_value
      - .offset:         176
        .size:           4
        .value_kind:     hidden_block_count_x
      - .offset:         180
        .size:           4
        .value_kind:     hidden_block_count_y
      - .offset:         184
        .size:           4
        .value_kind:     hidden_block_count_z
      - .offset:         188
        .size:           2
        .value_kind:     hidden_group_size_x
      - .offset:         190
        .size:           2
        .value_kind:     hidden_group_size_y
      - .offset:         192
        .size:           2
        .value_kind:     hidden_group_size_z
      - .offset:         194
        .size:           2
        .value_kind:     hidden_remainder_x
      - .offset:         196
        .size:           2
        .value_kind:     hidden_remainder_y
      - .offset:         198
        .size:           2
        .value_kind:     hidden_remainder_z
      - .offset:         216
        .size:           8
        .value_kind:     hidden_global_offset_x
      - .offset:         224
        .size:           8
        .value_kind:     hidden_global_offset_y
      - .offset:         232
        .size:           8
        .value_kind:     hidden_global_offset_z
      - .offset:         240
        .size:           2
        .value_kind:     hidden_grid_dims
      - .offset:         296
        .size:           4
        .value_kind:     hidden_dynamic_lds_size
    .group_segment_fixed_size: 0
    .kernarg_segment_align: 8
    .kernarg_segment_size: 432
    .language:       OpenCL C
    .language_version:
      - 2
      - 0
    .max_flat_workgroup_size: 512
    .name:           _Z3fwd4Args
    .private_segment_fixed_size: 0
    .sgpr_count:     104
    .sgpr_spill_count: 40
    .symbol:         _Z3fwd4Args.kd
    .uniform_work_group_size: 1
    .uses_dynamic_stack: false
    .vgpr_count:     250
    .vgpr_spill_count: 0
    .wavefront_size: 64
